# attn loop1: row-sum tree with v_pk_add_f32 (7 packed + 1 scalar add per softmax instead of 15 scalar adds)
# baseline (speedup 1.0000x reference)
.Lf_A:
	s_add_i32 s0, s0, 2
	ds_read_b128 v[102:105], v186 offset:18432
	ds_read_b128 v[106:109], v186 offset:27648
	ds_read_b128 v[110:113], v186 offset:18464
	ds_read_b128 v[86:89], v186 offset:27680
	ds_read_b128 v[90:93], v186 offset:18496
	ds_read_b128 v[172:175], v186 offset:27712
	ds_read_b128 v[72:75], v186 offset:18528
	v_exp_f32_e32 v2, v2
	v_exp_f32_e32 v18, v18
	s_waitcnt lgkmcnt(6)
	v_mfma_f32_32x32x16_f16 v[146:161], v[102:105], v[114:117], 0
	v_exp_f32_e32 v3, v3
	v_exp_f32_e32 v19, v19
	v_exp_f32_e32 v4, v4
	v_exp_f32_e32 v20, v20
	s_waitcnt lgkmcnt(5)
	v_mfma_f32_32x32x16_f16 v[34:49], v[106:109], v[130:133], 0
	v_exp_f32_e32 v5, v5
	v_exp_f32_e32 v21, v21
	v_exp_f32_e32 v6, v6
	v_exp_f32_e32 v22, v22
	s_waitcnt lgkmcnt(4)
	v_mfma_f32_32x32x16_f16 v[146:161], v[110:113], v[118:121], v[146:161]
	v_exp_f32_e32 v7, v7
	v_exp_f32_e32 v23, v23
	v_exp_f32_e32 v8, v8
	v_exp_f32_e32 v24, v24
	s_waitcnt lgkmcnt(3)
	v_mfma_f32_32x32x16_f16 v[34:49], v[86:89], v[134:137], v[34:49]
	v_exp_f32_e32 v9, v9
	v_exp_f32_e32 v25, v25
	s_waitcnt vmcnt(2)
	ds_write_b128 v185, v[162:165]
	ds_write_b128 v185, v[166:169] offset:9216
	ds_read_b128 v[238:241], v186 offset:27744
	s_min_u32 s12, s0, 27
	s_add_i32 s12, s18, s12
	s_lshl_b32 s12, s12, 13
	s_and_b32 s12, s12, 0x3e000
	s_add_u32 s28, s12, s3
	s_mov_b32 s29, 0
	v_lshl_add_u64 v[176:177], v[170:171], 0, s[12:13]
	global_load_dwordx4 v[162:165], v[176:177], off
	v_lshl_add_u64 v[176:177], v[170:171], 0, s[28:29]
	global_load_dwordx4 v[166:169], v[176:177], off
	v_exp_f32_e32 v10, v10
	v_exp_f32_e32 v26, v26
	v_exp_f32_e32 v11, v11
	v_exp_f32_e32 v27, v27
	s_waitcnt lgkmcnt(5)
	v_mfma_f32_32x32x16_f16 v[146:161], v[90:93], v[122:125], v[146:161]
	v_exp_f32_e32 v12, v12
	v_exp_f32_e32 v28, v28
	v_exp_f32_e32 v13, v13
	v_exp_f32_e32 v29, v29
	s_waitcnt lgkmcnt(4)
	v_mfma_f32_32x32x16_f16 v[34:49], v[172:175], v[138:141], v[34:49]
	v_exp_f32_e32 v14, v14
	v_exp_f32_e32 v30, v30
	v_exp_f32_e32 v15, v15
	v_exp_f32_e32 v31, v31
	s_waitcnt lgkmcnt(3)
	v_mfma_f32_32x32x16_f16 v[146:161], v[72:75], v[126:129], v[146:161]
	v_exp_f32_e32 v16, v16
	v_exp_f32_e32 v32, v32
	v_exp_f32_e32 v17, v17
	v_exp_f32_e32 v33, v33
	v_pk_add_f32 v[2:3], v[2:3], v[4:5]
	v_pk_add_f32 v[18:19], v[18:19], v[20:21]
	v_pk_add_f32 v[6:7], v[6:7], v[8:9]
	v_pk_add_f32 v[22:23], v[22:23], v[24:25]
	v_pk_add_f32 v[10:11], v[10:11], v[12:13]
	v_pk_add_f32 v[26:27], v[26:27], v[28:29]
	s_waitcnt lgkmcnt(0)
	v_mfma_f32_32x32x16_f16 v[34:49], v[238:241], v[142:145], v[34:49]
	v_pk_add_f32 v[14:15], v[14:15], v[16:17]
	v_pk_add_f32 v[30:31], v[30:31], v[32:33]
	v_pk_add_f32 v[2:3], v[2:3], v[6:7]
	v_pk_add_f32 v[18:19], v[18:19], v[22:23]
	v_pk_add_f32 v[10:11], v[10:11], v[14:15]
	v_pk_add_f32 v[26:27], v[26:27], v[30:31]
	v_pk_add_f32 v[2:3], v[2:3], v[10:11]
	v_pk_add_f32 v[18:19], v[18:19], v[26:27]
	v_add_f32_e32 v2, v2, v3
	v_add_f32_e32 v18, v18, v19
	v_add_f32_e32 v63, v63, v2
	v_add_f32_e32 v62, v62, v18
	s_waitcnt lgkmcnt(0)
	s_barrier
.Lf_B:
	ds_read_b128 v[102:105], v186
	ds_read_b128 v[106:109], v186 offset:9216
	ds_read_b128 v[110:113], v186 offset:32
	ds_read_b128 v[86:89], v186 offset:9248
	ds_read_b128 v[90:93], v186 offset:64
	ds_read_b128 v[172:175], v186 offset:9280
	ds_read_b128 v[72:75], v186 offset:96
	v_exp_f32_e32 v146, v146
	v_exp_f32_e32 v34, v34
	s_waitcnt lgkmcnt(6)
	v_mfma_f32_32x32x16_f16 v[2:17], v[102:105], v[114:117], 0
	v_exp_f32_e32 v147, v147
	v_exp_f32_e32 v35, v35
	v_exp_f32_e32 v148, v148
	v_exp_f32_e32 v36, v36
	s_waitcnt lgkmcnt(5)
	v_mfma_f32_32x32x16_f16 v[18:33], v[106:109], v[130:133], 0
	v_exp_f32_e32 v149, v149
	v_exp_f32_e32 v37, v37
	v_exp_f32_e32 v150, v150
	v_exp_f32_e32 v38, v38
	s_waitcnt lgkmcnt(4)
	v_mfma_f32_32x32x16_f16 v[2:17], v[110:113], v[118:121], v[2:17]
	v_exp_f32_e32 v151, v151
	v_exp_f32_e32 v39, v39
	v_exp_f32_e32 v152, v152
	v_exp_f32_e32 v40, v40
	s_waitcnt lgkmcnt(3)
	v_mfma_f32_32x32x16_f16 v[18:33], v[86:89], v[134:137], v[18:33]
	v_exp_f32_e32 v153, v153
	v_exp_f32_e32 v41, v41
	s_waitcnt vmcnt(2)
	ds_write_b128 v185, v[50:53] offset:18432
	ds_write_b128 v185, v[94:97] offset:27648
	ds_read_b128 v[238:241], v186 offset:9312
	s_min_u32 s12, s0, 26
	s_add_i32 s12, s17, s12
	s_add_i32 s12, s12, 2
	s_lshl_b32 s12, s12, 13
	s_and_b32 s12, s12, 0x3e000
	s_add_u32 s28, s12, s3
	s_mov_b32 s29, 0
	v_lshl_add_u64 v[176:177], v[170:171], 0, s[12:13]
	global_load_dwordx4 v[50:53], v[176:177], off
	v_lshl_add_u64 v[176:177], v[170:171], 0, s[28:29]
	global_load_dwordx4 v[94:97], v[176:177], off
	v_exp_f32_e32 v154, v154
	v_exp_f32_e32 v42, v42
	v_exp_f32_e32 v155, v155
	v_exp_f32_e32 v43, v43
	s_waitcnt lgkmcnt(5)
	v_mfma_f32_32x32x16_f16 v[2:17], v[90:93], v[122:125], v[2:17]
	v_exp_f32_e32 v156, v156
	v_exp_f32_e32 v44, v44
	v_exp_f32_e32 v157, v157
	v_exp_f32_e32 v45, v45
	s_waitcnt lgkmcnt(4)
	v_mfma_f32_32x32x16_f16 v[18:33], v[172:175], v[138:141], v[18:33]
	v_exp_f32_e32 v158, v158
	v_exp_f32_e32 v46, v46
	v_exp_f32_e32 v159, v159
	v_exp_f32_e32 v47, v47
	s_waitcnt lgkmcnt(3)
	v_mfma_f32_32x32x16_f16 v[2:17], v[72:75], v[126:129], v[2:17]
	v_exp_f32_e32 v160, v160
	v_exp_f32_e32 v48, v48
	v_exp_f32_e32 v161, v161
	v_exp_f32_e32 v49, v49
	v_pk_add_f32 v[146:147], v[146:147], v[148:149]
	v_pk_add_f32 v[34:35], v[34:35], v[36:37]
	v_pk_add_f32 v[150:151], v[150:151], v[152:153]
	v_pk_add_f32 v[38:39], v[38:39], v[40:41]
	v_pk_add_f32 v[154:155], v[154:155], v[156:157]
	v_pk_add_f32 v[42:43], v[42:43], v[44:45]
	s_waitcnt lgkmcnt(0)
	v_mfma_f32_32x32x16_f16 v[18:33], v[238:241], v[142:145], v[18:33]
	v_pk_add_f32 v[158:159], v[158:159], v[160:161]
	v_pk_add_f32 v[46:47], v[46:47], v[48:49]
	v_pk_add_f32 v[146:147], v[146:147], v[150:151]
	v_pk_add_f32 v[34:35], v[34:35], v[38:39]
	v_pk_add_f32 v[154:155], v[154:155], v[158:159]
	v_pk_add_f32 v[42:43], v[42:43], v[46:47]
	v_pk_add_f32 v[146:147], v[146:147], v[154:155]
	v_pk_add_f32 v[34:35], v[34:35], v[42:43]
	v_add_f32_e32 v146, v146, v147
	v_add_f32_e32 v34, v34, v35
	v_add_f32_e32 v63, v63, v146
	v_add_f32_e32 v62, v62, v34
	s_waitcnt lgkmcnt(0)
	s_barrier
	s_cmp_lt_u32 s0, 30
	s_cbranch_scc1 .Lf_A
	s_branch .Ll1_done
.Ls_A:
	s_add_i32 s0, s0, 2
	ds_read_b128 v[102:105], v186 offset:18432
	ds_read_b128 v[106:109], v186 offset:27648
	ds_read_b128 v[110:113], v186 offset:18464
	ds_read_b128 v[86:89], v186 offset:27680
	ds_read_b128 v[90:93], v186 offset:18496
	ds_read_b128 v[172:175], v186 offset:27712
	ds_read_b128 v[72:75], v186 offset:18528
	v_max3_f32 v76, v2, v3, v4
	v_max3_f32 v77, v18, v19, v20
	v_max3_f32 v76, v76, v5, v6
	v_max3_f32 v77, v77, v21, v22
	v_max3_f32 v76, v76, v7, v8
	v_max3_f32 v77, v77, v23, v24
	v_max3_f32 v76, v76, v9, v10
	v_max3_f32 v77, v77, v25, v26
	v_max3_f32 v76, v76, v11, v12
	v_max3_f32 v77, v77, v27, v28
	v_max3_f32 v76, v76, v13, v14
	v_max3_f32 v77, v77, v29, v30
	v_max3_f32 v76, v76, v15, v16
	v_max3_f32 v77, v77, v31, v32
	v_max_f32_e32 v76, v76, v17
	v_max_f32_e32 v77, v77, v33
	v_max_f32_e32 v85, v84, v76
	v_sub_f32_e32 v76, v84, v85
	v_exp_f32_e32 v76, v76
	v_mov_b32_e32 v84, v85
	v_sub_f32_e32 v2, v2, v85
	v_sub_f32_e32 v3, v3, v85
	v_sub_f32_e32 v4, v4, v85
	v_sub_f32_e32 v5, v5, v85
	v_sub_f32_e32 v6, v6, v85
	v_sub_f32_e32 v7, v7, v85
	v_sub_f32_e32 v8, v8, v85
	v_sub_f32_e32 v9, v9, v85
	v_sub_f32_e32 v10, v10, v85
	v_sub_f32_e32 v11, v11, v85
	v_sub_f32_e32 v12, v12, v85
	v_sub_f32_e32 v13, v13, v85
	v_sub_f32_e32 v14, v14, v85
	v_sub_f32_e32 v15, v15, v85
	v_sub_f32_e32 v16, v16, v85
	v_sub_f32_e32 v17, v17, v85
	v_max_f32_e32 v85, v83, v77
	v_sub_f32_e32 v77, v83, v85
	v_exp_f32_e32 v77, v77
	v_mov_b32_e32 v83, v85
	v_sub_f32_e32 v18, v18, v85
	v_sub_f32_e32 v19, v19, v85
	v_sub_f32_e32 v20, v20, v85
	v_sub_f32_e32 v21, v21, v85
	v_sub_f32_e32 v22, v22, v85
	v_sub_f32_e32 v23, v23, v85
	v_sub_f32_e32 v24, v24, v85
	v_sub_f32_e32 v25, v25, v85
	v_sub_f32_e32 v26, v26, v85
	v_sub_f32_e32 v27, v27, v85
	v_sub_f32_e32 v28, v28, v85
	v_sub_f32_e32 v29, v29, v85
	v_sub_f32_e32 v30, v30, v85
	v_sub_f32_e32 v31, v31, v85
	v_sub_f32_e32 v32, v32, v85
	v_sub_f32_e32 v33, v33, v85
	v_exp_f32_e32 v2, v2
	v_exp_f32_e32 v18, v18
	s_waitcnt lgkmcnt(6)
	v_mfma_f32_32x32x16_f16 v[146:161], v[102:105], v[114:117], 0
	v_exp_f32_e32 v3, v3
	v_exp_f32_e32 v19, v19
	v_exp_f32_e32 v4, v4
	v_exp_f32_e32 v20, v20
	s_waitcnt lgkmcnt(5)
	v_mfma_f32_32x32x16_f16 v[34:49], v[106:109], v[130:133], 0
	v_exp_f32_e32 v5, v5
	v_exp_f32_e32 v21, v21
	v_exp_f32_e32 v6, v6
	v_exp_f32_e32 v22, v22
	s_waitcnt lgkmcnt(4)
	v_mfma_f32_32x32x16_f16 v[146:161], v[110:113], v[118:121], v[146:161]
	v_exp_f32_e32 v7, v7
	v_exp_f32_e32 v23, v23
	v_exp_f32_e32 v8, v8
	v_exp_f32_e32 v24, v24
	s_waitcnt lgkmcnt(3)
	v_mfma_f32_32x32x16_f16 v[34:49], v[86:89], v[134:137], v[34:49]
	v_exp_f32_e32 v9, v9
	v_exp_f32_e32 v25, v25
	s_waitcnt vmcnt(2)
	ds_write_b128 v185, v[162:165]
	ds_write_b128 v185, v[166:169] offset:9216
	ds_read_b128 v[238:241], v186 offset:27744
	s_min_u32 s12, s0, 27
	s_add_i32 s12, s18, s12
	s_lshl_b32 s12, s12, 13
	s_and_b32 s12, s12, 0x3e000
	s_add_u32 s28, s12, s3
	s_mov_b32 s29, 0
	v_lshl_add_u64 v[176:177], v[170:171], 0, s[12:13]
	global_load_dwordx4 v[162:165], v[176:177], off
	v_lshl_add_u64 v[176:177], v[170:171], 0, s[28:29]
	global_load_dwordx4 v[166:169], v[176:177], off
	v_exp_f32_e32 v10, v10
	v_exp_f32_e32 v26, v26
	v_exp_f32_e32 v11, v11
	v_exp_f32_e32 v27, v27
	s_waitcnt lgkmcnt(5)
	v_mfma_f32_32x32x16_f16 v[146:161], v[90:93], v[122:125], v[146:161]
	v_exp_f32_e32 v12, v12
	v_exp_f32_e32 v28, v28
	v_exp_f32_e32 v13, v13
	v_exp_f32_e32 v29, v29
	s_waitcnt lgkmcnt(4)
	v_mfma_f32_32x32x16_f16 v[34:49], v[172:175], v[138:141], v[34:49]
	v_exp_f32_e32 v14, v14
	v_exp_f32_e32 v30, v30
	v_exp_f32_e32 v15, v15
	v_exp_f32_e32 v31, v31
	s_waitcnt lgkmcnt(3)
	v_mfma_f32_32x32x16_f16 v[146:161], v[72:75], v[126:129], v[146:161]
	v_exp_f32_e32 v16, v16
	v_exp_f32_e32 v32, v32
	v_exp_f32_e32 v17, v17
	v_exp_f32_e32 v33, v33
	v_pk_add_f32 v[2:3], v[2:3], v[4:5]
	v_pk_add_f32 v[18:19], v[18:19], v[20:21]
	v_pk_add_f32 v[6:7], v[6:7], v[8:9]
	v_pk_add_f32 v[22:23], v[22:23], v[24:25]
	v_pk_add_f32 v[10:11], v[10:11], v[12:13]
	v_pk_add_f32 v[26:27], v[26:27], v[28:29]
	s_waitcnt lgkmcnt(0)
	v_mfma_f32_32x32x16_f16 v[34:49], v[238:241], v[142:145], v[34:49]
	v_pk_add_f32 v[14:15], v[14:15], v[16:17]
	v_pk_add_f32 v[30:31], v[30:31], v[32:33]
	v_pk_add_f32 v[2:3], v[2:3], v[6:7]
	v_pk_add_f32 v[18:19], v[18:19], v[22:23]
	v_pk_add_f32 v[10:11], v[10:11], v[14:15]
	v_pk_add_f32 v[26:27], v[26:27], v[30:31]
	v_pk_add_f32 v[2:3], v[2:3], v[10:11]
	v_pk_add_f32 v[18:19], v[18:19], v[26:27]
	v_add_f32_e32 v2, v2, v3
	v_add_f32_e32 v18, v18, v19
	v_fma_f32 v63, v63, v76, v2
	v_fma_f32 v62, v62, v77, v18
	s_waitcnt lgkmcnt(0)
	s_barrier
.Ls_B:
	ds_read_b128 v[102:105], v186
	ds_read_b128 v[106:109], v186 offset:9216
	ds_read_b128 v[110:113], v186 offset:32
	ds_read_b128 v[86:89], v186 offset:9248
	ds_read_b128 v[90:93], v186 offset:64
	ds_read_b128 v[172:175], v186 offset:9280
	ds_read_b128 v[72:75], v186 offset:96
	v_max3_f32 v76, v146, v147, v148
	v_max3_f32 v77, v34, v35, v36
	v_max3_f32 v76, v76, v149, v150
	v_max3_f32 v77, v77, v37, v38
	v_max3_f32 v76, v76, v151, v152
	v_max3_f32 v77, v77, v39, v40
	v_max3_f32 v76, v76, v153, v154
	v_max3_f32 v77, v77, v41, v42
	v_max3_f32 v76, v76, v155, v156
	v_max3_f32 v77, v77, v43, v44
	v_max3_f32 v76, v76, v157, v158
	v_max3_f32 v77, v77, v45, v46
	v_max3_f32 v76, v76, v159, v160
	v_max3_f32 v77, v77, v47, v48
	v_max_f32_e32 v76, v76, v161
	v_max_f32_e32 v77, v77, v49
	v_max_f32_e32 v85, v84, v76
	v_sub_f32_e32 v76, v84, v85
	v_exp_f32_e32 v76, v76
	v_mov_b32_e32 v84, v85
	v_sub_f32_e32 v146, v146, v85
	v_sub_f32_e32 v147, v147, v85
	v_sub_f32_e32 v148, v148, v85
	v_sub_f32_e32 v149, v149, v85
	v_sub_f32_e32 v150, v150, v85
	v_sub_f32_e32 v151, v151, v85
	v_sub_f32_e32 v152, v152, v85
	v_sub_f32_e32 v153, v153, v85
	v_sub_f32_e32 v154, v154, v85
	v_sub_f32_e32 v155, v155, v85
	v_sub_f32_e32 v156, v156, v85
	v_sub_f32_e32 v157, v157, v85
	v_sub_f32_e32 v158, v158, v85
	v_sub_f32_e32 v159, v159, v85
	v_sub_f32_e32 v160, v160, v85
	v_sub_f32_e32 v161, v161, v85
	v_max_f32_e32 v85, v83, v77
	v_sub_f32_e32 v77, v83, v85
	v_exp_f32_e32 v77, v77
	v_mov_b32_e32 v83, v85
	v_sub_f32_e32 v34, v34, v85
	v_sub_f32_e32 v35, v35, v85
	v_sub_f32_e32 v36, v36, v85
	v_sub_f32_e32 v37, v37, v85
	v_sub_f32_e32 v38, v38, v85
	v_sub_f32_e32 v39, v39, v85
	v_sub_f32_e32 v40, v40, v85
	v_sub_f32_e32 v41, v41, v85
	v_sub_f32_e32 v42, v42, v85
	v_sub_f32_e32 v43, v43, v85
	v_sub_f32_e32 v44, v44, v85
	v_sub_f32_e32 v45, v45, v85
	v_sub_f32_e32 v46, v46, v85
	v_sub_f32_e32 v47, v47, v85
	v_sub_f32_e32 v48, v48, v85
	v_sub_f32_e32 v49, v49, v85
	v_exp_f32_e32 v146, v146
	v_exp_f32_e32 v34, v34
	s_waitcnt lgkmcnt(6)
	v_mfma_f32_32x32x16_f16 v[2:17], v[102:105], v[114:117], 0
	v_exp_f32_e32 v147, v147
	v_exp_f32_e32 v35, v35
	v_exp_f32_e32 v148, v148
	v_exp_f32_e32 v36, v36
	s_waitcnt lgkmcnt(5)
	v_mfma_f32_32x32x16_f16 v[18:33], v[106:109], v[130:133], 0
	v_exp_f32_e32 v149, v149
	v_exp_f32_e32 v37, v37
	v_exp_f32_e32 v150, v150
	v_exp_f32_e32 v38, v38
	s_waitcnt lgkmcnt(4)
	v_mfma_f32_32x32x16_f16 v[2:17], v[110:113], v[118:121], v[2:17]
	v_exp_f32_e32 v151, v151
	v_exp_f32_e32 v39, v39
	v_exp_f32_e32 v152, v152
	v_exp_f32_e32 v40, v40
	s_waitcnt lgkmcnt(3)
	v_mfma_f32_32x32x16_f16 v[18:33], v[86:89], v[134:137], v[18:33]
	v_exp_f32_e32 v153, v153
	v_exp_f32_e32 v41, v41
	s_waitcnt vmcnt(2)
	ds_write_b128 v185, v[50:53] offset:18432
	ds_write_b128 v185, v[94:97] offset:27648
	ds_read_b128 v[238:241], v186 offset:9312
	s_min_u32 s12, s0, 26
	s_add_i32 s12, s17, s12
	s_add_i32 s12, s12, 2
	s_lshl_b32 s12, s12, 13
	s_and_b32 s12, s12, 0x3e000
	s_add_u32 s28, s12, s3
	s_mov_b32 s29, 0
	v_lshl_add_u64 v[176:177], v[170:171], 0, s[12:13]
	global_load_dwordx4 v[50:53], v[176:177], off
	v_lshl_add_u64 v[176:177], v[170:171], 0, s[28:29]
	global_load_dwordx4 v[94:97], v[176:177], off
	v_exp_f32_e32 v154, v154
	v_exp_f32_e32 v42, v42
	v_exp_f32_e32 v155, v155
	v_exp_f32_e32 v43, v43
	s_waitcnt lgkmcnt(5)
	v_mfma_f32_32x32x16_f16 v[2:17], v[90:93], v[122:125], v[2:17]
	v_exp_f32_e32 v156, v156
	v_exp_f32_e32 v44, v44
	v_exp_f32_e32 v157, v157
	v_exp_f32_e32 v45, v45
	s_waitcnt lgkmcnt(4)
	v_mfma_f32_32x32x16_f16 v[18:33], v[172:175], v[138:141], v[18:33]
	v_exp_f32_e32 v158, v158
	v_exp_f32_e32 v46, v46
	v_exp_f32_e32 v159, v159
	v_exp_f32_e32 v47, v47
	s_waitcnt lgkmcnt(3)
	v_mfma_f32_32x32x16_f16 v[2:17], v[72:75], v[126:129], v[2:17]
	v_exp_f32_e32 v160, v160
	v_exp_f32_e32 v48, v48
	v_exp_f32_e32 v161, v161
	v_exp_f32_e32 v49, v49
	v_pk_add_f32 v[146:147], v[146:147], v[148:149]
	v_pk_add_f32 v[34:35], v[34:35], v[36:37]
	v_pk_add_f32 v[150:151], v[150:151], v[152:153]
	v_pk_add_f32 v[38:39], v[38:39], v[40:41]
	v_pk_add_f32 v[154:155], v[154:155], v[156:157]
	v_pk_add_f32 v[42:43], v[42:43], v[44:45]
	s_waitcnt lgkmcnt(0)
	v_mfma_f32_32x32x16_f16 v[18:33], v[238:241], v[142:145], v[18:33]
	v_pk_add_f32 v[158:159], v[158:159], v[160:161]
	v_pk_add_f32 v[46:47], v[46:47], v[48:49]
	v_pk_add_f32 v[146:147], v[146:147], v[150:151]
	v_pk_add_f32 v[34:35], v[34:35], v[38:39]
	v_pk_add_f32 v[154:155], v[154:155], v[158:159]
	v_pk_add_f32 v[42:43], v[42:43], v[46:47]
	v_pk_add_f32 v[146:147], v[146:147], v[154:155]
	v_pk_add_f32 v[34:35], v[34:35], v[42:43]
	v_add_f32_e32 v146, v146, v147
	v_add_f32_e32 v34, v34, v35
	v_fma_f32 v63, v63, v76, v146
	v_fma_f32 v62, v62, v77, v34
	s_waitcnt lgkmcnt(0)
	s_barrier
	s_cmp_lt_u32 s0, 30
	s_cbranch_scc1 .Ls_A
